# P6 epilogue: gate loads and PART loads both non-temporal
# speedup vs baseline: 1.0099x; 1.0099x over previous
; __device__ __forceinline__ void unpack8(const v4u w, float (&o)[8]) { o[0] = bflo(w.x); o[1] = bfhi(w.x); o[2] = bflo(w.y); o[3] = bfhi(w.y); o[4] = bflo(w.z); o[5] = bfhi(w.z); o[6] = bflo(w.w); o[7] = bfhi(w.w); }
; __device__ __forceinline__ v4u pack8(const float (&o)[8]) { v4u w; w.x = pk2(o[0], o[1]); w.y = pk2(o[2], o[3]); w.z = pk2(o[4], o[5]); w.w = pk2(o[6], o[7]); return w; }
; __device__ __forceinline__ float sigmf(float x) { return __builtin_amdgcn_rcpf(1.f + __expf(-x)); }
;     __device__ __forceinline__ void operator()(const f32x4 (&acc)[2][2][4][2], const pg8::Unit& u, int wr, int wc, int fr, int fq_in) const {
;     ...
;         const int row0 = u.pm * 256 + wr * 64 + fr, col0 = u.pn * 256 + wc * 32 + 8 * fq; const bool first = u.sel == 0; const int goff = first ? 0 : D;
; #pragma unroll
;         for (int bj = 0; bj < 2; ++bj) {
;             const int col = col0 + bj * 128;
;             float b0[8];
;             { const f32x4 t0 = *(const f32x4*)(bg + goff + col), t1 = *(const f32x4*)(bg + goff + col + 4);
; #pragma unroll
;               for (int q = 0; q < 4; ++q) { b0[q] = t0[q]; b0[4 + q] = t1[q]; } }
; #pragma unroll
;             for (int ai = 0; ai < 2; ++ai) {
;                 v4u gw_[4], pw_[4];
; #pragma unroll
;                 for (int m = 0; m < 4; ++m) { const size_t row = (size_t)(row0 + ai * 128 + m * 16);
;                     gw_[m] = *(const v4u*)(Gt + row * (2 * D) + goff + col); pw_[m] = first ? (v4u){0u, 0u, 0u, 0u} : *(const v4u*)(O + row * D + col); }
;                 __builtin_amdgcn_sched_barrier(0);
; #pragma unroll
;                 for (int m = 0; m < 4; ++m) { const size_t row = (size_t)(row0 + ai * 128 + m * 16);
;                     float g0[8], p[8]; unpack8(gw_[m], g0); unpack8(pw_[m], p);
;                     float o[8];
; #pragma unroll
;                     for (int q = 0; q < 4; ++q) { o[q] = p[q] + sigmf(g0[q] + b0[q]) * acc[ai][bj][m][0][q]; o[4 + q] = p[4 + q] + sigmf(g0[4 + q] + b0[4 + q]) * acc[ai][bj][m][1][q]; }
;                     *(v4u*)(O + row * D + col) = pack8(o); }
.Lepi6_second:
	global_load_dwordx4 v[244:247], v252, s[0:1]
	global_load_dwordx4 v[248:251], v252, s[0:1] offset:16
	global_load_dwordx4 v[114:117], v227, s[98:99] nt
	global_load_dwordx4 v[228:231], v226, s[4:5] nt
	v_add_u32_e32 v254, 0x4000, v227
	global_load_dwordx4 v[118:121], v254, s[98:99] nt
	v_add_u32_e32 v253, 0x10000, v226
	global_load_dwordx4 v[232:235], v253, s[4:5] nt
	v_add_u32_e32 v254, 0x8000, v227
	global_load_dwordx4 v[138:141], v254, s[98:99] nt
	v_add_u32_e32 v253, 0x20000, v226
	global_load_dwordx4 v[236:239], v253, s[4:5] nt
	v_add_u32_e32 v254, 0xc000, v227
	global_load_dwordx4 v[142:145], v254, s[98:99] nt
	v_add_u32_e32 v253, 0x30000, v226
	global_load_dwordx4 v[240:243], v253, s[4:5] nt
	v_add_u32_e32 v254, 0x10000, v227
	global_load_dwordx4 v[146:149], v254, s[98:99] nt
	v_add_u32_e32 v254, 0x14000, v227
	global_load_dwordx4 v[150:153], v254, s[98:99] nt
	v_add_u32_e32 v254, 0x18000, v227
	global_load_dwordx4 v[154:157], v254, s[98:99] nt
	v_add_u32_e32 v254, 0x1c000, v227
	global_load_dwordx4 v[158:161], v254, s[98:99] nt
	v_add_u32_e32 v254, 0x2000, v227
	global_load_dwordx4 v[162:165], v254, s[98:99] nt
	v_add_u32_e32 v254, 0x6000, v227
	global_load_dwordx4 v[166:169], v254, s[98:99] nt
	v_add_u32_e32 v254, 0xa000, v227
	global_load_dwordx4 v[190:193], v254, s[98:99] nt
	v_add_u32_e32 v254, 0xe000, v227
	global_load_dwordx4 v[194:197], v254, s[98:99] nt
	v_add_u32_e32 v254, 0x12000, v227
	global_load_dwordx4 v[198:201], v254, s[98:99] nt
	v_add_u32_e32 v254, 0x16000, v227
	global_load_dwordx4 v[202:205], v254, s[98:99] nt
	v_add_u32_e32 v254, 0x1a000, v227
	global_load_dwordx4 v[206:209], v254, s[98:99] nt
	v_add_u32_e32 v254, 0x1e000, v227
	global_load_dwordx4 v[210:213], v254, s[98:99] nt
	s_waitcnt vmcnt(20)
	s_waitcnt vmcnt(19)
	v_lshlrev_b32_e32 v170, 16, v114
	v_and_b32_e32 v114, 0xffff0000, v114
	v_lshlrev_b32_e32 v171, 16, v115
	v_and_b32_e32 v115, 0xffff0000, v115
	v_lshlrev_b32_e32 v214, 16, v116
	v_and_b32_e32 v116, 0xffff0000, v116
	v_lshlrev_b32_e32 v215, 16, v117
	v_and_b32_e32 v117, 0xffff0000, v117
	v_add_f32_e32 v170, v244, v170
	v_add_f32_e32 v114, v245, v114
	v_add_f32_e32 v171, v246, v171
	v_add_f32_e32 v115, v247, v115
	v_add_f32_e32 v214, v248, v214
	v_add_f32_e32 v116, v249, v116
	v_add_f32_e32 v215, v250, v215
	v_add_f32_e32 v117, v251, v117
	v_mul_f32_e32 v170, 0xbfb8aa3b, v170
	v_mul_f32_e32 v114, 0xbfb8aa3b, v114
	v_mul_f32_e32 v171, 0xbfb8aa3b, v171
	v_mul_f32_e32 v115, 0xbfb8aa3b, v115
	v_mul_f32_e32 v214, 0xbfb8aa3b, v214
	v_mul_f32_e32 v116, 0xbfb8aa3b, v116
	v_mul_f32_e32 v215, 0xbfb8aa3b, v215
	v_mul_f32_e32 v117, 0xbfb8aa3b, v117
	v_exp_f32_e32 v170, v170
	v_exp_f32_e32 v114, v114
	v_exp_f32_e32 v171, v171
	v_exp_f32_e32 v115, v115
	v_exp_f32_e32 v214, v214
	v_exp_f32_e32 v116, v116
	v_exp_f32_e32 v215, v215
	v_exp_f32_e32 v117, v117
	v_add_f32_e32 v170, 1.0, v170
	v_add_f32_e32 v114, 1.0, v114
	v_add_f32_e32 v171, 1.0, v171
	v_add_f32_e32 v115, 1.0, v115
	v_add_f32_e32 v214, 1.0, v214
	v_add_f32_e32 v116, 1.0, v116
	v_add_f32_e32 v215, 1.0, v215
	v_add_f32_e32 v117, 1.0, v117
	v_rcp_f32_e32 v170, v170
	v_rcp_f32_e32 v114, v114
	v_rcp_f32_e32 v171, v171
	v_rcp_f32_e32 v115, v115
	v_rcp_f32_e32 v214, v214
	v_rcp_f32_e32 v116, v116
	v_rcp_f32_e32 v215, v215
	v_rcp_f32_e32 v117, v117
	s_waitcnt vmcnt(18)
	v_lshlrev_b32_e32 v221, 16, v228
	v_and_b32_e32 v228, 0xffff0000, v228
	v_lshlrev_b32_e32 v222, 16, v229
	v_and_b32_e32 v229, 0xffff0000, v229
	v_lshlrev_b32_e32 v223, 16, v230
	v_and_b32_e32 v230, 0xffff0000, v230
	v_lshlrev_b32_e32 v224, 16, v231
	v_and_b32_e32 v231, 0xffff0000, v231
	v_fma_f32 v134, v134, v170, v221
	v_fma_f32 v135, v135, v114, v228
	v_fma_f32 v136, v136, v171, v222
	v_fma_f32 v137, v137, v115, v229
	v_fma_f32 v130, v130, v214, v223
	v_fma_f32 v131, v131, v116, v230
	v_fma_f32 v132, v132, v215, v224
	v_fma_f32 v133, v133, v117, v231
	v_cvt_pk_bf16_f32 v134, v134, v135
	v_cvt_pk_bf16_f32 v135, v136, v137
	v_cvt_pk_bf16_f32 v136, v130, v131
	v_cvt_pk_bf16_f32 v137, v132, v133
	v_add_u32_e32 v253, 0x80000, v226
	global_load_dwordx4 v[228:231], v253, s[4:5] nt
	global_store_dwordx4 v226, v[134:137], s[4:5]
	s_waitcnt vmcnt(19)
	v_lshlrev_b32_e32 v170, 16, v118
	v_and_b32_e32 v118, 0xffff0000, v118
	v_lshlrev_b32_e32 v171, 16, v119
	v_and_b32_e32 v119, 0xffff0000, v119
	v_lshlrev_b32_e32 v214, 16, v120
	v_and_b32_e32 v120, 0xffff0000, v120
	v_lshlrev_b32_e32 v215, 16, v121
	v_and_b32_e32 v121, 0xffff0000, v121
	v_add_f32_e32 v170, v244, v170
	v_add_f32_e32 v118, v245, v118
	v_add_f32_e32 v171, v246, v171
	v_add_f32_e32 v119, v247, v119
	v_add_f32_e32 v214, v248, v214
	v_add_f32_e32 v120, v249, v120
	v_add_f32_e32 v215, v250, v215
	v_add_f32_e32 v121, v251, v121
	v_mul_f32_e32 v170, 0xbfb8aa3b, v170
	v_mul_f32_e32 v118, 0xbfb8aa3b, v118
	v_mul_f32_e32 v171, 0xbfb8aa3b, v171
	v_mul_f32_e32 v119, 0xbfb8aa3b, v119
	v_mul_f32_e32 v214, 0xbfb8aa3b, v214
	v_mul_f32_e32 v120, 0xbfb8aa3b, v120
	v_mul_f32_e32 v215, 0xbfb8aa3b, v215
	v_mul_f32_e32 v121, 0xbfb8aa3b, v121
	v_exp_f32_e32 v170, v170
	v_exp_f32_e32 v118, v118
	v_exp_f32_e32 v171, v171
	v_exp_f32_e32 v119, v119
	v_exp_f32_e32 v214, v214
	v_exp_f32_e32 v120, v120
	v_exp_f32_e32 v215, v215
	v_exp_f32_e32 v121, v121
	v_add_f32_e32 v170, 1.0, v170
	v_add_f32_e32 v118, 1.0, v118
	v_add_f32_e32 v171, 1.0, v171
	v_add_f32_e32 v119, 1.0, v119
	v_add_f32_e32 v214, 1.0, v214
	v_add_f32_e32 v120, 1.0, v120
	v_add_f32_e32 v215, 1.0, v215
	v_add_f32_e32 v121, 1.0, v121
	v_rcp_f32_e32 v170, v170
	v_rcp_f32_e32 v118, v118
	v_rcp_f32_e32 v171, v171
	v_rcp_f32_e32 v119, v119
	v_rcp_f32_e32 v214, v214
	v_rcp_f32_e32 v120, v120
	v_rcp_f32_e32 v215, v215
	v_rcp_f32_e32 v121, v121
	s_waitcnt vmcnt(18)
; __device__ __forceinline__ void unpack8(const v4u w, float (&o)[8]) { o[0] = bflo(w.x); o[1] = bfhi(w.x); o[2] = bflo(w.y); o[3] = bfhi(w.y); o[4] = bflo(w.z); o[5] = bfhi(w.z); o[6] = bflo(w.w); o[7] = bfhi(w.w); }
; __device__ __forceinline__ v4u pack8(const float (&o)[8]) { v4u w; w.x = pk2(o[0], o[1]); w.y = pk2(o[2], o[3]); w.z = pk2(o[4], o[5]); w.w = pk2(o[6], o[7]); return w; }
; __device__ __forceinline__ float sigmf(float x) { return __builtin_amdgcn_rcpf(1.f + __expf(-x)); }
;     __device__ __forceinline__ void operator()(const f32x4 (&acc)[2][2][4][2], const pg8::Unit& u, int wr, int wc, int fr, int fq_in) const {
;     ...
;                 for (int m = 0; m < 4; ++m) { const size_t row = (size_t)(row0 + ai * 128 + m * 16);
;                     gw_[m] = *(const v4u*)(Gt + row * (2 * D) + goff + col); pw_[m] = first ? (v4u){0u, 0u, 0u, 0u} : *(const v4u*)(O + row * D + col); }
;                 __builtin_amdgcn_sched_barrier(0);
; #pragma unroll
;                 for (int m = 0; m < 4; ++m) { const size_t row = (size_t)(row0 + ai * 128 + m * 16);
;                     float g0[8], p[8]; unpack8(gw_[m], g0); unpack8(pw_[m], p);
;                     float o[8];
; #pragma unroll
;                     for (int q = 0; q < 4; ++q) { o[q] = p[q] + sigmf(g0[q] + b0[q]) * acc[ai][bj][m][0][q]; o[4 + q] = p[4 + q] + sigmf(g0[4 + q] + b0[4 + q]) * acc[ai][bj][m][1][q]; }
;                     *(v4u*)(O + row * D + col) = pack8(o); }
	v_lshlrev_b32_e32 v221, 16, v232
	v_and_b32_e32 v232, 0xffff0000, v232
	v_lshlrev_b32_e32 v222, 16, v233
	v_and_b32_e32 v233, 0xffff0000, v233
	v_lshlrev_b32_e32 v223, 16, v234
	v_and_b32_e32 v234, 0xffff0000, v234
	v_lshlrev_b32_e32 v224, 16, v235
	v_and_b32_e32 v235, 0xffff0000, v235
	v_fma_f32 v126, v126, v170, v221
	v_fma_f32 v127, v127, v118, v232
	v_fma_f32 v128, v128, v171, v222
	v_fma_f32 v129, v129, v119, v233
	v_fma_f32 v122, v122, v214, v223
	v_fma_f32 v123, v123, v120, v234
	v_fma_f32 v124, v124, v215, v224
	v_fma_f32 v125, v125, v121, v235
	v_cvt_pk_bf16_f32 v126, v126, v127
	v_cvt_pk_bf16_f32 v127, v128, v129
	v_cvt_pk_bf16_f32 v128, v122, v123
	v_cvt_pk_bf16_f32 v129, v124, v125
	v_add_u32_e32 v253, 0x90000, v226
	global_load_dwordx4 v[232:235], v253, s[4:5] nt
	v_add_u32_e32 v225, 0x10000, v226
	global_store_dwordx4 v225, v[126:129], s[4:5]
	global_load_dwordx4 v[130:133], v252, s[0:1] offset:512
	global_load_dwordx4 v[122:125], v252, s[0:1] offset:528
	s_waitcnt vmcnt(21)
	v_lshlrev_b32_e32 v170, 16, v138
	v_and_b32_e32 v138, 0xffff0000, v138
	v_lshlrev_b32_e32 v171, 16, v139
	v_and_b32_e32 v139, 0xffff0000, v139
	v_lshlrev_b32_e32 v214, 16, v140
	v_and_b32_e32 v140, 0xffff0000, v140
	v_lshlrev_b32_e32 v215, 16, v141
	v_and_b32_e32 v141, 0xffff0000, v141
	v_add_f32_e32 v170, v244, v170
	v_add_f32_e32 v138, v245, v138
	v_add_f32_e32 v171, v246, v171
	v_add_f32_e32 v139, v247, v139
	v_add_f32_e32 v214, v248, v214
	v_add_f32_e32 v140, v249, v140
	v_add_f32_e32 v215, v250, v215
	v_add_f32_e32 v141, v251, v141
	v_mul_f32_e32 v170, 0xbfb8aa3b, v170
	v_mul_f32_e32 v138, 0xbfb8aa3b, v138
	v_mul_f32_e32 v171, 0xbfb8aa3b, v171
	v_mul_f32_e32 v139, 0xbfb8aa3b, v139
	v_mul_f32_e32 v214, 0xbfb8aa3b, v214
	v_mul_f32_e32 v140, 0xbfb8aa3b, v140
	v_mul_f32_e32 v215, 0xbfb8aa3b, v215
	v_mul_f32_e32 v141, 0xbfb8aa3b, v141
	v_exp_f32_e32 v170, v170
	v_exp_f32_e32 v138, v138
	v_exp_f32_e32 v171, v171
	v_exp_f32_e32 v139, v139
	v_exp_f32_e32 v214, v214
	v_exp_f32_e32 v140, v140
	v_exp_f32_e32 v215, v215
	v_exp_f32_e32 v141, v141
	v_add_f32_e32 v170, 1.0, v170
	v_add_f32_e32 v138, 1.0, v138
	v_add_f32_e32 v171, 1.0, v171
	v_add_f32_e32 v139, 1.0, v139
	v_add_f32_e32 v214, 1.0, v214
	v_add_f32_e32 v140, 1.0, v140
	v_add_f32_e32 v215, 1.0, v215
	v_add_f32_e32 v141, 1.0, v141
	v_rcp_f32_e32 v170, v170
	v_rcp_f32_e32 v138, v138
	v_rcp_f32_e32 v171, v171
	v_rcp_f32_e32 v139, v139
	v_rcp_f32_e32 v214, v214
	v_rcp_f32_e32 v140, v140
	v_rcp_f32_e32 v215, v215
	v_rcp_f32_e32 v141, v141
	s_waitcnt vmcnt(20)
	v_lshlrev_b32_e32 v221, 16, v236
	v_and_b32_e32 v236, 0xffff0000, v236
	v_lshlrev_b32_e32 v222, 16, v237
	v_and_b32_e32 v237, 0xffff0000, v237
	v_lshlrev_b32_e32 v223, 16, v238
	v_and_b32_e32 v238, 0xffff0000, v238
	v_lshlrev_b32_e32 v224, 16, v239
	v_and_b32_e32 v239, 0xffff0000, v239
	v_fma_f32 v110, v110, v170, v221
	v_fma_f32 v111, v111, v138, v236
	v_fma_f32 v112, v112, v171, v222
	v_fma_f32 v113, v113, v139, v237
	v_fma_f32 v106, v106, v214, v223
	v_fma_f32 v107, v107, v140, v238
	v_fma_f32 v108, v108, v215, v224
	v_fma_f32 v109, v109, v141, v239
	v_cvt_pk_bf16_f32 v110, v110, v111
	v_cvt_pk_bf16_f32 v111, v112, v113
	v_cvt_pk_bf16_f32 v112, v106, v107
	v_cvt_pk_bf16_f32 v113, v108, v109
	v_add_u32_e32 v253, 0xa0000, v226
	global_load_dwordx4 v[236:239], v253, s[4:5] nt
	v_add_u32_e32 v225, 0x20000, v226
	global_store_dwordx4 v225, v[110:113], s[4:5]
	s_waitcnt vmcnt(21)
	v_lshlrev_b32_e32 v170, 16, v142
	v_and_b32_e32 v142, 0xffff0000, v142
	v_lshlrev_b32_e32 v171, 16, v143
	v_and_b32_e32 v143, 0xffff0000, v143
	v_lshlrev_b32_e32 v214, 16, v144
	v_and_b32_e32 v144, 0xffff0000, v144
	v_lshlrev_b32_e32 v215, 16, v145
	v_and_b32_e32 v145, 0xffff0000, v145
	v_add_f32_e32 v170, v244, v170
	v_add_f32_e32 v142, v245, v142
	v_add_f32_e32 v171, v246, v171
	v_add_f32_e32 v143, v247, v143
	v_add_f32_e32 v214, v248, v214
	v_add_f32_e32 v144, v249, v144
	v_add_f32_e32 v215, v250, v215
	v_add_f32_e32 v145, v251, v145
	v_mul_f32_e32 v170, 0xbfb8aa3b, v170
	v_mul_f32_e32 v142, 0xbfb8aa3b, v142
	v_mul_f32_e32 v171, 0xbfb8aa3b, v171
	v_mul_f32_e32 v143, 0xbfb8aa3b, v143
	v_mul_f32_e32 v214, 0xbfb8aa3b, v214
	v_mul_f32_e32 v144, 0xbfb8aa3b, v144
	v_mul_f32_e32 v215, 0xbfb8aa3b, v215
	v_mul_f32_e32 v145, 0xbfb8aa3b, v145
	v_exp_f32_e32 v170, v170
	v_exp_f32_e32 v142, v142
	v_exp_f32_e32 v171, v171
	v_exp_f32_e32 v143, v143
	v_exp_f32_e32 v214, v214
	v_exp_f32_e32 v144, v144
	v_exp_f32_e32 v215, v215
	v_exp_f32_e32 v145, v145
	v_add_f32_e32 v170, 1.0, v170
	v_add_f32_e32 v142, 1.0, v142
	v_add_f32_e32 v171, 1.0, v171
	v_add_f32_e32 v143, 1.0, v143
	v_add_f32_e32 v214, 1.0, v214
	v_add_f32_e32 v144, 1.0, v144
	v_add_f32_e32 v215, 1.0, v215
	v_add_f32_e32 v145, 1.0, v145
	v_rcp_f32_e32 v170, v170
	v_rcp_f32_e32 v142, v142
	v_rcp_f32_e32 v171, v171
	v_rcp_f32_e32 v143, v143
	v_rcp_f32_e32 v214, v214
	v_rcp_f32_e32 v144, v144
	v_rcp_f32_e32 v215, v215
	v_rcp_f32_e32 v145, v145
	s_waitcnt vmcnt(20)
	v_lshlrev_b32_e32 v221, 16, v240
	v_and_b32_e32 v240, 0xffff0000, v240
	v_lshlrev_b32_e32 v222, 16, v241
	v_and_b32_e32 v241, 0xffff0000, v241
	v_lshlrev_b32_e32 v223, 16, v242
	v_and_b32_e32 v242, 0xffff0000, v242
	v_lshlrev_b32_e32 v224, 16, v243
	v_and_b32_e32 v243, 0xffff0000, v243
	v_fma_f32 v102, v102, v170, v221
	v_fma_f32 v103, v103, v142, v240
	v_fma_f32 v104, v104, v171, v222
	v_fma_f32 v105, v105, v143, v241
	v_fma_f32 v98, v98, v214, v223
	v_fma_f32 v99, v99, v144, v242
	v_fma_f32 v100, v100, v215, v224
	v_fma_f32 v101, v101, v145, v243
	v_cvt_pk_bf16_f32 v102, v102, v103
	v_cvt_pk_bf16_f32 v103, v104, v105
	v_cvt_pk_bf16_f32 v104, v98, v99
	v_cvt_pk_bf16_f32 v105, v100, v101
	v_add_u32_e32 v253, 0xb0000, v226
	global_load_dwordx4 v[240:243], v253, s[4:5] nt
	v_add_u32_e32 v225, 0x30000, v226
	global_store_dwordx4 v225, v[102:105], s[4:5]
	s_waitcnt vmcnt(21)
; __device__ __forceinline__ void unpack8(const v4u w, float (&o)[8]) { o[0] = bflo(w.x); o[1] = bfhi(w.x); o[2] = bflo(w.y); o[3] = bfhi(w.y); o[4] = bflo(w.z); o[5] = bfhi(w.z); o[6] = bflo(w.w); o[7] = bfhi(w.w); }
; __device__ __forceinline__ v4u pack8(const float (&o)[8]) { v4u w; w.x = pk2(o[0], o[1]); w.y = pk2(o[2], o[3]); w.z = pk2(o[4], o[5]); w.w = pk2(o[6], o[7]); return w; }
; __device__ __forceinline__ float sigmf(float x) { return __builtin_amdgcn_rcpf(1.f + __expf(-x)); }
;     __device__ __forceinline__ void operator()(const f32x4 (&acc)[2][2][4][2], const pg8::Unit& u, int wr, int wc, int fr, int fq_in) const {
;     ...
;                 for (int m = 0; m < 4; ++m) { const size_t row = (size_t)(row0 + ai * 128 + m * 16);
;                     gw_[m] = *(const v4u*)(Gt + row * (2 * D) + goff + col); pw_[m] = first ? (v4u){0u, 0u, 0u, 0u} : *(const v4u*)(O + row * D + col); }
;                 __builtin_amdgcn_sched_barrier(0);
; #pragma unroll
;                 for (int m = 0; m < 4; ++m) { const size_t row = (size_t)(row0 + ai * 128 + m * 16);
;                     float g0[8], p[8]; unpack8(gw_[m], g0); unpack8(pw_[m], p);
;                     float o[8];
; #pragma unroll
;                     for (int q = 0; q < 4; ++q) { o[q] = p[q] + sigmf(g0[q] + b0[q]) * acc[ai][bj][m][0][q]; o[4 + q] = p[4 + q] + sigmf(g0[4 + q] + b0[4 + q]) * acc[ai][bj][m][1][q]; }
;                     *(v4u*)(O + row * D + col) = pack8(o); }
	v_lshlrev_b32_e32 v170, 16, v146
	v_and_b32_e32 v146, 0xffff0000, v146
	v_lshlrev_b32_e32 v171, 16, v147
	v_and_b32_e32 v147, 0xffff0000, v147
	v_lshlrev_b32_e32 v214, 16, v148
	v_and_b32_e32 v148, 0xffff0000, v148
	v_lshlrev_b32_e32 v215, 16, v149
	v_and_b32_e32 v149, 0xffff0000, v149
	v_add_f32_e32 v170, v244, v170
	v_add_f32_e32 v146, v245, v146
	v_add_f32_e32 v171, v246, v171
	v_add_f32_e32 v147, v247, v147
	v_add_f32_e32 v214, v248, v214
	v_add_f32_e32 v148, v249, v148
	v_add_f32_e32 v215, v250, v215
	v_add_f32_e32 v149, v251, v149
	v_mul_f32_e32 v170, 0xbfb8aa3b, v170
	v_mul_f32_e32 v146, 0xbfb8aa3b, v146
	v_mul_f32_e32 v171, 0xbfb8aa3b, v171
	v_mul_f32_e32 v147, 0xbfb8aa3b, v147
	v_mul_f32_e32 v214, 0xbfb8aa3b, v214
	v_mul_f32_e32 v148, 0xbfb8aa3b, v148
	v_mul_f32_e32 v215, 0xbfb8aa3b, v215
	v_mul_f32_e32 v149, 0xbfb8aa3b, v149
	v_exp_f32_e32 v170, v170
	v_exp_f32_e32 v146, v146
	v_exp_f32_e32 v171, v171
	v_exp_f32_e32 v147, v147
	v_exp_f32_e32 v214, v214
	v_exp_f32_e32 v148, v148
	v_exp_f32_e32 v215, v215
	v_exp_f32_e32 v149, v149
	v_add_f32_e32 v170, 1.0, v170
	v_add_f32_e32 v146, 1.0, v146
	v_add_f32_e32 v171, 1.0, v171
	v_add_f32_e32 v147, 1.0, v147
	v_add_f32_e32 v214, 1.0, v214
	v_add_f32_e32 v148, 1.0, v148
	v_add_f32_e32 v215, 1.0, v215
	v_add_f32_e32 v149, 1.0, v149
	v_rcp_f32_e32 v170, v170
	v_rcp_f32_e32 v146, v146
	v_rcp_f32_e32 v171, v171
	v_rcp_f32_e32 v147, v147
	v_rcp_f32_e32 v214, v214
	v_rcp_f32_e32 v148, v148
	v_rcp_f32_e32 v215, v215
	v_rcp_f32_e32 v149, v149
	s_waitcnt vmcnt(9)
	v_lshlrev_b32_e32 v221, 16, v228
	v_and_b32_e32 v228, 0xffff0000, v228
	v_lshlrev_b32_e32 v222, 16, v229
	v_and_b32_e32 v229, 0xffff0000, v229
	v_lshlrev_b32_e32 v223, 16, v230
	v_and_b32_e32 v230, 0xffff0000, v230
	v_lshlrev_b32_e32 v224, 16, v231
	v_and_b32_e32 v231, 0xffff0000, v231
	v_fma_f32 v94, v94, v170, v221
	v_fma_f32 v95, v95, v146, v228
	v_fma_f32 v96, v96, v171, v222
	v_fma_f32 v97, v97, v147, v229
	v_fma_f32 v90, v90, v214, v223
	v_fma_f32 v91, v91, v148, v230
	v_fma_f32 v92, v92, v215, v224
	v_fma_f32 v93, v93, v149, v231
	v_cvt_pk_bf16_f32 v94, v94, v95
	v_cvt_pk_bf16_f32 v95, v96, v97
	v_cvt_pk_bf16_f32 v96, v90, v91
	v_cvt_pk_bf16_f32 v97, v92, v93
	global_load_dwordx4 v[228:231], v226, s[4:5] offset:256 nt
	v_add_u32_e32 v225, 0x80000, v226
	global_store_dwordx4 v225, v[94:97], s[4:5]
	s_waitcnt vmcnt(22)
	v_lshlrev_b32_e32 v170, 16, v150
	v_and_b32_e32 v150, 0xffff0000, v150
	v_lshlrev_b32_e32 v171, 16, v151
	v_and_b32_e32 v151, 0xffff0000, v151
	v_lshlrev_b32_e32 v214, 16, v152
	v_and_b32_e32 v152, 0xffff0000, v152
	v_lshlrev_b32_e32 v215, 16, v153
	v_and_b32_e32 v153, 0xffff0000, v153
	v_add_f32_e32 v170, v244, v170
	v_add_f32_e32 v150, v245, v150
	v_add_f32_e32 v171, v246, v171
	v_add_f32_e32 v151, v247, v151
	v_add_f32_e32 v214, v248, v214
	v_add_f32_e32 v152, v249, v152
	v_add_f32_e32 v215, v250, v215
	v_add_f32_e32 v153, v251, v153
	v_mul_f32_e32 v170, 0xbfb8aa3b, v170
	v_mul_f32_e32 v150, 0xbfb8aa3b, v150
	v_mul_f32_e32 v171, 0xbfb8aa3b, v171
	v_mul_f32_e32 v151, 0xbfb8aa3b, v151
	v_mul_f32_e32 v214, 0xbfb8aa3b, v214
	v_mul_f32_e32 v152, 0xbfb8aa3b, v152
	v_mul_f32_e32 v215, 0xbfb8aa3b, v215
	v_mul_f32_e32 v153, 0xbfb8aa3b, v153
	v_exp_f32_e32 v170, v170
	v_exp_f32_e32 v150, v150
	v_exp_f32_e32 v171, v171
	v_exp_f32_e32 v151, v151
	v_exp_f32_e32 v214, v214
	v_exp_f32_e32 v152, v152
	v_exp_f32_e32 v215, v215
	v_exp_f32_e32 v153, v153
	v_add_f32_e32 v170, 1.0, v170
	v_add_f32_e32 v150, 1.0, v150
	v_add_f32_e32 v171, 1.0, v171
	v_add_f32_e32 v151, 1.0, v151
	v_add_f32_e32 v214, 1.0, v214
	v_add_f32_e32 v152, 1.0, v152
	v_add_f32_e32 v215, 1.0, v215
	v_add_f32_e32 v153, 1.0, v153
	v_rcp_f32_e32 v170, v170
	v_rcp_f32_e32 v150, v150
	v_rcp_f32_e32 v171, v171
	v_rcp_f32_e32 v151, v151
	v_rcp_f32_e32 v214, v214
	v_rcp_f32_e32 v152, v152
	v_rcp_f32_e32 v215, v215
	v_rcp_f32_e32 v153, v153
	s_waitcnt vmcnt(9)
	v_lshlrev_b32_e32 v221, 16, v232
	v_and_b32_e32 v232, 0xffff0000, v232
	v_lshlrev_b32_e32 v222, 16, v233
	v_and_b32_e32 v233, 0xffff0000, v233
	v_lshlrev_b32_e32 v223, 16, v234
	v_and_b32_e32 v234, 0xffff0000, v234
	v_lshlrev_b32_e32 v224, 16, v235
	v_and_b32_e32 v235, 0xffff0000, v235
	v_fma_f32 v86, v86, v170, v221
	v_fma_f32 v87, v87, v150, v232
	v_fma_f32 v88, v88, v171, v222
	v_fma_f32 v89, v89, v151, v233
	v_fma_f32 v82, v82, v214, v223
	v_fma_f32 v83, v83, v152, v234
	v_fma_f32 v84, v84, v215, v224
	v_fma_f32 v85, v85, v153, v235
	v_cvt_pk_bf16_f32 v86, v86, v87
	v_cvt_pk_bf16_f32 v87, v88, v89
	v_cvt_pk_bf16_f32 v88, v82, v83
	v_cvt_pk_bf16_f32 v89, v84, v85
	v_add_u32_e32 v253, 0x10000, v226
	global_load_dwordx4 v[232:235], v253, s[4:5] offset:256 nt
	v_add_u32_e32 v225, 0x90000, v226
	global_store_dwordx4 v225, v[86:89], s[4:5]
	s_waitcnt vmcnt(23)
	v_lshlrev_b32_e32 v170, 16, v154
	v_and_b32_e32 v154, 0xffff0000, v154
	v_lshlrev_b32_e32 v171, 16, v155
	v_and_b32_e32 v155, 0xffff0000, v155
	v_lshlrev_b32_e32 v214, 16, v156
	v_and_b32_e32 v156, 0xffff0000, v156
	v_lshlrev_b32_e32 v215, 16, v157
	v_and_b32_e32 v157, 0xffff0000, v157
	v_add_f32_e32 v170, v244, v170
	v_add_f32_e32 v154, v245, v154
	v_add_f32_e32 v171, v246, v171
	v_add_f32_e32 v155, v247, v155
	v_add_f32_e32 v214, v248, v214
	v_add_f32_e32 v156, v249, v156
	v_add_f32_e32 v215, v250, v215
	v_add_f32_e32 v157, v251, v157
	v_mul_f32_e32 v170, 0xbfb8aa3b, v170
	v_mul_f32_e32 v154, 0xbfb8aa3b, v154
	v_mul_f32_e32 v171, 0xbfb8aa3b, v171
	v_mul_f32_e32 v155, 0xbfb8aa3b, v155
	v_mul_f32_e32 v214, 0xbfb8aa3b, v214
	v_mul_f32_e32 v156, 0xbfb8aa3b, v156
	v_mul_f32_e32 v215, 0xbfb8aa3b, v215
	v_mul_f32_e32 v157, 0xbfb8aa3b, v157
	v_exp_f32_e32 v170, v170
	v_exp_f32_e32 v154, v154
	v_exp_f32_e32 v171, v171
	v_exp_f32_e32 v155, v155
	v_exp_f32_e32 v214, v214
	v_exp_f32_e32 v156, v156
	v_exp_f32_e32 v215, v215
	v_exp_f32_e32 v157, v157
	v_add_f32_e32 v170, 1.0, v170
	v_add_f32_e32 v154, 1.0, v154
	v_add_f32_e32 v171, 1.0, v171
	v_add_f32_e32 v155, 1.0, v155
	v_add_f32_e32 v214, 1.0, v214
	v_add_f32_e32 v156, 1.0, v156
	v_add_f32_e32 v215, 1.0, v215
	v_add_f32_e32 v157, 1.0, v157
	v_rcp_f32_e32 v170, v170
	v_rcp_f32_e32 v154, v154
	v_rcp_f32_e32 v171, v171
	v_rcp_f32_e32 v155, v155
	v_rcp_f32_e32 v214, v214
	v_rcp_f32_e32 v156, v156
	v_rcp_f32_e32 v215, v215
	v_rcp_f32_e32 v157, v157
	s_waitcnt vmcnt(7)
; __device__ __forceinline__ void unpack8(const v4u w, float (&o)[8]) { o[0] = bflo(w.x); o[1] = bfhi(w.x); o[2] = bflo(w.y); o[3] = bfhi(w.y); o[4] = bflo(w.z); o[5] = bfhi(w.z); o[6] = bflo(w.w); o[7] = bfhi(w.w); }
; __device__ __forceinline__ v4u pack8(const float (&o)[8]) { v4u w; w.x = pk2(o[0], o[1]); w.y = pk2(o[2], o[3]); w.z = pk2(o[4], o[5]); w.w = pk2(o[6], o[7]); return w; }
; __device__ __forceinline__ float sigmf(float x) { return __builtin_amdgcn_rcpf(1.f + __expf(-x)); }
;     __device__ __forceinline__ void operator()(const f32x4 (&acc)[2][2][4][2], const pg8::Unit& u, int wr, int wc, int fr, int fq_in) const {
;     ...
;                 for (int m = 0; m < 4; ++m) { const size_t row = (size_t)(row0 + ai * 128 + m * 16);
;                     gw_[m] = *(const v4u*)(Gt + row * (2 * D) + goff + col); pw_[m] = first ? (v4u){0u, 0u, 0u, 0u} : *(const v4u*)(O + row * D + col); }
;                 __builtin_amdgcn_sched_barrier(0);
; #pragma unroll
;                 for (int m = 0; m < 4; ++m) { const size_t row = (size_t)(row0 + ai * 128 + m * 16);
;                     float g0[8], p[8]; unpack8(gw_[m], g0); unpack8(pw_[m], p);
;                     float o[8];
; #pragma unroll
;                     for (int q = 0; q < 4; ++q) { o[q] = p[q] + sigmf(g0[q] + b0[q]) * acc[ai][bj][m][0][q]; o[4 + q] = p[4 + q] + sigmf(g0[4 + q] + b0[4 + q]) * acc[ai][bj][m][1][q]; }
;                     *(v4u*)(O + row * D + col) = pack8(o); }
	v_lshlrev_b32_e32 v221, 16, v236
	v_and_b32_e32 v236, 0xffff0000, v236
	v_lshlrev_b32_e32 v222, 16, v237
	v_and_b32_e32 v237, 0xffff0000, v237
	v_lshlrev_b32_e32 v223, 16, v238
	v_and_b32_e32 v238, 0xffff0000, v238
	v_lshlrev_b32_e32 v224, 16, v239
	v_and_b32_e32 v239, 0xffff0000, v239
	v_fma_f32 v78, v78, v170, v221
	v_fma_f32 v79, v79, v154, v236
	v_fma_f32 v80, v80, v171, v222
	v_fma_f32 v81, v81, v155, v237
	v_fma_f32 v74, v74, v214, v223
	v_fma_f32 v75, v75, v156, v238
	v_fma_f32 v76, v76, v215, v224
	v_fma_f32 v77, v77, v157, v239
	v_cvt_pk_bf16_f32 v78, v78, v79
	v_cvt_pk_bf16_f32 v79, v80, v81
	v_cvt_pk_bf16_f32 v80, v74, v75
	v_cvt_pk_bf16_f32 v81, v76, v77
	v_add_u32_e32 v253, 0x20000, v226
	global_load_dwordx4 v[236:239], v253, s[4:5] offset:256 nt
	v_add_u32_e32 v225, 0xa0000, v226
	global_store_dwordx4 v225, v[78:81], s[4:5]
	s_waitcnt vmcnt(24)
	v_lshlrev_b32_e32 v170, 16, v158
	v_and_b32_e32 v158, 0xffff0000, v158
	v_lshlrev_b32_e32 v171, 16, v159
	v_and_b32_e32 v159, 0xffff0000, v159
	v_lshlrev_b32_e32 v214, 16, v160
	v_and_b32_e32 v160, 0xffff0000, v160
	v_lshlrev_b32_e32 v215, 16, v161
	v_and_b32_e32 v161, 0xffff0000, v161
	v_add_f32_e32 v170, v244, v170
	v_add_f32_e32 v158, v245, v158
	v_add_f32_e32 v171, v246, v171
	v_add_f32_e32 v159, v247, v159
	v_add_f32_e32 v214, v248, v214
	v_add_f32_e32 v160, v249, v160
	v_add_f32_e32 v215, v250, v215
	v_add_f32_e32 v161, v251, v161
	v_mul_f32_e32 v170, 0xbfb8aa3b, v170
	v_mul_f32_e32 v158, 0xbfb8aa3b, v158
	v_mul_f32_e32 v171, 0xbfb8aa3b, v171
	v_mul_f32_e32 v159, 0xbfb8aa3b, v159
	v_mul_f32_e32 v214, 0xbfb8aa3b, v214
	v_mul_f32_e32 v160, 0xbfb8aa3b, v160
	v_mul_f32_e32 v215, 0xbfb8aa3b, v215
	v_mul_f32_e32 v161, 0xbfb8aa3b, v161
	v_exp_f32_e32 v170, v170
	v_exp_f32_e32 v158, v158
	v_exp_f32_e32 v171, v171
	v_exp_f32_e32 v159, v159
	v_exp_f32_e32 v214, v214
	v_exp_f32_e32 v160, v160
	v_exp_f32_e32 v215, v215
	v_exp_f32_e32 v161, v161
	v_add_f32_e32 v170, 1.0, v170
	v_add_f32_e32 v158, 1.0, v158
	v_add_f32_e32 v171, 1.0, v171
	v_add_f32_e32 v159, 1.0, v159
	v_add_f32_e32 v214, 1.0, v214
	v_add_f32_e32 v160, 1.0, v160
	v_add_f32_e32 v215, 1.0, v215
	v_add_f32_e32 v161, 1.0, v161
	v_rcp_f32_e32 v170, v170
	v_rcp_f32_e32 v158, v158
	v_rcp_f32_e32 v171, v171
	v_rcp_f32_e32 v159, v159
	v_rcp_f32_e32 v214, v214
	v_rcp_f32_e32 v160, v160
	v_rcp_f32_e32 v215, v215
	v_rcp_f32_e32 v161, v161
	s_waitcnt vmcnt(7)
	v_lshlrev_b32_e32 v221, 16, v240
	v_and_b32_e32 v240, 0xffff0000, v240
	v_lshlrev_b32_e32 v222, 16, v241
	v_and_b32_e32 v241, 0xffff0000, v241
	v_lshlrev_b32_e32 v223, 16, v242
	v_and_b32_e32 v242, 0xffff0000, v242
	v_lshlrev_b32_e32 v224, 16, v243
	v_and_b32_e32 v243, 0xffff0000, v243
	v_fma_f32 v70, v70, v170, v221
	v_fma_f32 v71, v71, v158, v240
	v_fma_f32 v72, v72, v171, v222
	v_fma_f32 v73, v73, v159, v241
	v_fma_f32 v66, v66, v214, v223
	v_fma_f32 v67, v67, v160, v242
	v_fma_f32 v68, v68, v215, v224
	v_fma_f32 v69, v69, v161, v243
	v_cvt_pk_bf16_f32 v70, v70, v71
	v_cvt_pk_bf16_f32 v71, v72, v73
	v_cvt_pk_bf16_f32 v72, v66, v67
	v_cvt_pk_bf16_f32 v73, v68, v69
	v_add_u32_e32 v253, 0x30000, v226
	global_load_dwordx4 v[240:243], v253, s[4:5] offset:256 nt
	v_add_u32_e32 v225, 0xb0000, v226
	global_store_dwordx4 v225, v[70:73], s[4:5]
	s_waitcnt vmcnt(12)
	s_waitcnt vmcnt(25)
	v_lshlrev_b32_e32 v170, 16, v162
	v_and_b32_e32 v162, 0xffff0000, v162
	v_lshlrev_b32_e32 v171, 16, v163
	v_and_b32_e32 v163, 0xffff0000, v163
	v_lshlrev_b32_e32 v214, 16, v164
	v_and_b32_e32 v164, 0xffff0000, v164
	v_lshlrev_b32_e32 v215, 16, v165
	v_and_b32_e32 v165, 0xffff0000, v165
	v_add_f32_e32 v170, v130, v170
	v_add_f32_e32 v162, v131, v162
	v_add_f32_e32 v171, v132, v171
	v_add_f32_e32 v163, v133, v163
	v_add_f32_e32 v214, v122, v214
	v_add_f32_e32 v164, v123, v164
	v_add_f32_e32 v215, v124, v215
	v_add_f32_e32 v165, v125, v165
	v_mul_f32_e32 v170, 0xbfb8aa3b, v170
	v_mul_f32_e32 v162, 0xbfb8aa3b, v162
	v_mul_f32_e32 v171, 0xbfb8aa3b, v171
	v_mul_f32_e32 v163, 0xbfb8aa3b, v163
	v_mul_f32_e32 v214, 0xbfb8aa3b, v214
	v_mul_f32_e32 v164, 0xbfb8aa3b, v164
	v_mul_f32_e32 v215, 0xbfb8aa3b, v215
	v_mul_f32_e32 v165, 0xbfb8aa3b, v165
	v_exp_f32_e32 v170, v170
	v_exp_f32_e32 v162, v162
	v_exp_f32_e32 v171, v171
	v_exp_f32_e32 v163, v163
	v_exp_f32_e32 v214, v214
	v_exp_f32_e32 v164, v164
	v_exp_f32_e32 v215, v215
	v_exp_f32_e32 v165, v165
	v_add_f32_e32 v170, 1.0, v170
	v_add_f32_e32 v162, 1.0, v162
	v_add_f32_e32 v171, 1.0, v171
	v_add_f32_e32 v163, 1.0, v163
	v_add_f32_e32 v214, 1.0, v214
	v_add_f32_e32 v164, 1.0, v164
	v_add_f32_e32 v215, 1.0, v215
	v_add_f32_e32 v165, 1.0, v165
	v_rcp_f32_e32 v170, v170
	v_rcp_f32_e32 v162, v162
	v_rcp_f32_e32 v171, v171
	v_rcp_f32_e32 v163, v163
	v_rcp_f32_e32 v214, v214
	v_rcp_f32_e32 v164, v164
	v_rcp_f32_e32 v215, v215
	v_rcp_f32_e32 v165, v165
	s_waitcnt vmcnt(7)
	v_lshlrev_b32_e32 v221, 16, v228
	v_and_b32_e32 v228, 0xffff0000, v228
	v_lshlrev_b32_e32 v222, 16, v229
	v_and_b32_e32 v229, 0xffff0000, v229
	v_lshlrev_b32_e32 v223, 16, v230
	v_and_b32_e32 v230, 0xffff0000, v230
	v_lshlrev_b32_e32 v224, 16, v231
	v_and_b32_e32 v231, 0xffff0000, v231
	v_fma_f32 v62, v62, v170, v221
	v_fma_f32 v63, v63, v162, v228
	v_fma_f32 v64, v64, v171, v222
	v_fma_f32 v65, v65, v163, v229
	v_fma_f32 v58, v58, v214, v223
	v_fma_f32 v59, v59, v164, v230
	v_fma_f32 v60, v60, v215, v224
	v_fma_f32 v61, v61, v165, v231
	v_cvt_pk_bf16_f32 v62, v62, v63
	v_cvt_pk_bf16_f32 v63, v64, v65
	v_cvt_pk_bf16_f32 v64, v58, v59
	v_cvt_pk_bf16_f32 v65, v60, v61
	v_add_u32_e32 v253, 0x80000, v226
	global_load_dwordx4 v[228:231], v253, s[4:5] offset:256 nt
	global_store_dwordx4 v226, v[62:65], s[4:5] offset:256
	s_waitcnt vmcnt(26)
; __device__ __forceinline__ void unpack8(const v4u w, float (&o)[8]) { o[0] = bflo(w.x); o[1] = bfhi(w.x); o[2] = bflo(w.y); o[3] = bfhi(w.y); o[4] = bflo(w.z); o[5] = bfhi(w.z); o[6] = bflo(w.w); o[7] = bfhi(w.w); }
; __device__ __forceinline__ v4u pack8(const float (&o)[8]) { v4u w; w.x = pk2(o[0], o[1]); w.y = pk2(o[2], o[3]); w.z = pk2(o[4], o[5]); w.w = pk2(o[6], o[7]); return w; }
; __device__ __forceinline__ float sigmf(float x) { return __builtin_amdgcn_rcpf(1.f + __expf(-x)); }
;     __device__ __forceinline__ void operator()(const f32x4 (&acc)[2][2][4][2], const pg8::Unit& u, int wr, int wc, int fr, int fq_in) const {
;     ...
;                 for (int m = 0; m < 4; ++m) { const size_t row = (size_t)(row0 + ai * 128 + m * 16);
;                     gw_[m] = *(const v4u*)(Gt + row * (2 * D) + goff + col); pw_[m] = first ? (v4u){0u, 0u, 0u, 0u} : *(const v4u*)(O + row * D + col); }
;                 __builtin_amdgcn_sched_barrier(0);
; #pragma unroll
;                 for (int m = 0; m < 4; ++m) { const size_t row = (size_t)(row0 + ai * 128 + m * 16);
;                     float g0[8], p[8]; unpack8(gw_[m], g0); unpack8(pw_[m], p);
;                     float o[8];
; #pragma unroll
;                     for (int q = 0; q < 4; ++q) { o[q] = p[q] + sigmf(g0[q] + b0[q]) * acc[ai][bj][m][0][q]; o[4 + q] = p[4 + q] + sigmf(g0[4 + q] + b0[4 + q]) * acc[ai][bj][m][1][q]; }
;                     *(v4u*)(O + row * D + col) = pack8(o); }
	v_lshlrev_b32_e32 v170, 16, v166
	v_and_b32_e32 v166, 0xffff0000, v166
	v_lshlrev_b32_e32 v171, 16, v167
	v_and_b32_e32 v167, 0xffff0000, v167
	v_lshlrev_b32_e32 v214, 16, v168
	v_and_b32_e32 v168, 0xffff0000, v168
	v_lshlrev_b32_e32 v215, 16, v169
	v_and_b32_e32 v169, 0xffff0000, v169
	v_add_f32_e32 v170, v130, v170
	v_add_f32_e32 v166, v131, v166
	v_add_f32_e32 v171, v132, v171
	v_add_f32_e32 v167, v133, v167
	v_add_f32_e32 v214, v122, v214
	v_add_f32_e32 v168, v123, v168
	v_add_f32_e32 v215, v124, v215
	v_add_f32_e32 v169, v125, v169
	v_mul_f32_e32 v170, 0xbfb8aa3b, v170
	v_mul_f32_e32 v166, 0xbfb8aa3b, v166
	v_mul_f32_e32 v171, 0xbfb8aa3b, v171
	v_mul_f32_e32 v167, 0xbfb8aa3b, v167
	v_mul_f32_e32 v214, 0xbfb8aa3b, v214
	v_mul_f32_e32 v168, 0xbfb8aa3b, v168
	v_mul_f32_e32 v215, 0xbfb8aa3b, v215
	v_mul_f32_e32 v169, 0xbfb8aa3b, v169
	v_exp_f32_e32 v170, v170
	v_exp_f32_e32 v166, v166
	v_exp_f32_e32 v171, v171
	v_exp_f32_e32 v167, v167
	v_exp_f32_e32 v214, v214
	v_exp_f32_e32 v168, v168
	v_exp_f32_e32 v215, v215
	v_exp_f32_e32 v169, v169
	v_add_f32_e32 v170, 1.0, v170
	v_add_f32_e32 v166, 1.0, v166
	v_add_f32_e32 v171, 1.0, v171
	v_add_f32_e32 v167, 1.0, v167
	v_add_f32_e32 v214, 1.0, v214
	v_add_f32_e32 v168, 1.0, v168
	v_add_f32_e32 v215, 1.0, v215
	v_add_f32_e32 v169, 1.0, v169
	v_rcp_f32_e32 v170, v170
	v_rcp_f32_e32 v166, v166
	v_rcp_f32_e32 v171, v171
	v_rcp_f32_e32 v167, v167
	v_rcp_f32_e32 v214, v214
	v_rcp_f32_e32 v168, v168
	v_rcp_f32_e32 v215, v215
	v_rcp_f32_e32 v169, v169
	s_waitcnt vmcnt(7)
	v_lshlrev_b32_e32 v221, 16, v232
	v_and_b32_e32 v232, 0xffff0000, v232
	v_lshlrev_b32_e32 v222, 16, v233
	v_and_b32_e32 v233, 0xffff0000, v233
	v_lshlrev_b32_e32 v223, 16, v234
	v_and_b32_e32 v234, 0xffff0000, v234
	v_lshlrev_b32_e32 v224, 16, v235
	v_and_b32_e32 v235, 0xffff0000, v235
	v_fma_f32 v54, v54, v170, v221
	v_fma_f32 v55, v55, v166, v232
	v_fma_f32 v56, v56, v171, v222
	v_fma_f32 v57, v57, v167, v233
	v_fma_f32 v50, v50, v214, v223
	v_fma_f32 v51, v51, v168, v234
	v_fma_f32 v52, v52, v215, v224
	v_fma_f32 v53, v53, v169, v235
	v_cvt_pk_bf16_f32 v54, v54, v55
	v_cvt_pk_bf16_f32 v55, v56, v57
	v_cvt_pk_bf16_f32 v56, v50, v51
	v_cvt_pk_bf16_f32 v57, v52, v53
	v_add_u32_e32 v253, 0x90000, v226
	global_load_dwordx4 v[232:235], v253, s[4:5] offset:256 nt
	v_add_u32_e32 v225, 0x10000, v226
	global_store_dwordx4 v225, v[54:57], s[4:5] offset:256
	s_waitcnt vmcnt(27)
	v_lshlrev_b32_e32 v170, 16, v190
	v_and_b32_e32 v190, 0xffff0000, v190
	v_lshlrev_b32_e32 v171, 16, v191
	v_and_b32_e32 v191, 0xffff0000, v191
	v_lshlrev_b32_e32 v214, 16, v192
	v_and_b32_e32 v192, 0xffff0000, v192
	v_lshlrev_b32_e32 v215, 16, v193
	v_and_b32_e32 v193, 0xffff0000, v193
	v_add_f32_e32 v170, v130, v170
	v_add_f32_e32 v190, v131, v190
	v_add_f32_e32 v171, v132, v171
	v_add_f32_e32 v191, v133, v191
	v_add_f32_e32 v214, v122, v214
	v_add_f32_e32 v192, v123, v192
	v_add_f32_e32 v215, v124, v215
	v_add_f32_e32 v193, v125, v193
	v_mul_f32_e32 v170, 0xbfb8aa3b, v170
	v_mul_f32_e32 v190, 0xbfb8aa3b, v190
	v_mul_f32_e32 v171, 0xbfb8aa3b, v171
	v_mul_f32_e32 v191, 0xbfb8aa3b, v191
	v_mul_f32_e32 v214, 0xbfb8aa3b, v214
	v_mul_f32_e32 v192, 0xbfb8aa3b, v192
	v_mul_f32_e32 v215, 0xbfb8aa3b, v215
	v_mul_f32_e32 v193, 0xbfb8aa3b, v193
	v_exp_f32_e32 v170, v170
	v_exp_f32_e32 v190, v190
	v_exp_f32_e32 v171, v171
	v_exp_f32_e32 v191, v191
	v_exp_f32_e32 v214, v214
	v_exp_f32_e32 v192, v192
	v_exp_f32_e32 v215, v215
	v_exp_f32_e32 v193, v193
	v_add_f32_e32 v170, 1.0, v170
	v_add_f32_e32 v190, 1.0, v190
	v_add_f32_e32 v171, 1.0, v171
	v_add_f32_e32 v191, 1.0, v191
	v_add_f32_e32 v214, 1.0, v214
	v_add_f32_e32 v192, 1.0, v192
	v_add_f32_e32 v215, 1.0, v215
	v_add_f32_e32 v193, 1.0, v193
	v_rcp_f32_e32 v170, v170
	v_rcp_f32_e32 v190, v190
	v_rcp_f32_e32 v171, v171
	v_rcp_f32_e32 v191, v191
	v_rcp_f32_e32 v214, v214
	v_rcp_f32_e32 v192, v192
	v_rcp_f32_e32 v215, v215
	v_rcp_f32_e32 v193, v193
	s_waitcnt vmcnt(7)
	v_lshlrev_b32_e32 v221, 16, v236
	v_and_b32_e32 v236, 0xffff0000, v236
	v_lshlrev_b32_e32 v222, 16, v237
	v_and_b32_e32 v237, 0xffff0000, v237
	v_lshlrev_b32_e32 v223, 16, v238
	v_and_b32_e32 v238, 0xffff0000, v238
	v_lshlrev_b32_e32 v224, 16, v239
	v_and_b32_e32 v239, 0xffff0000, v239
	v_fma_f32 v46, v46, v170, v221
	v_fma_f32 v47, v47, v190, v236
	v_fma_f32 v48, v48, v171, v222
	v_fma_f32 v49, v49, v191, v237
	v_fma_f32 v42, v42, v214, v223
	v_fma_f32 v43, v43, v192, v238
	v_fma_f32 v44, v44, v215, v224
	v_fma_f32 v45, v45, v193, v239
	v_cvt_pk_bf16_f32 v46, v46, v47
	v_cvt_pk_bf16_f32 v47, v48, v49
	v_cvt_pk_bf16_f32 v48, v42, v43
	v_cvt_pk_bf16_f32 v49, v44, v45
	v_add_u32_e32 v253, 0xa0000, v226
	global_load_dwordx4 v[236:239], v253, s[4:5] offset:256 nt
	v_add_u32_e32 v225, 0x20000, v226
	global_store_dwordx4 v225, v[46:49], s[4:5] offset:256
	s_waitcnt vmcnt(28)
	v_lshlrev_b32_e32 v170, 16, v194
	v_and_b32_e32 v194, 0xffff0000, v194
	v_lshlrev_b32_e32 v171, 16, v195
	v_and_b32_e32 v195, 0xffff0000, v195
	v_lshlrev_b32_e32 v214, 16, v196
	v_and_b32_e32 v196, 0xffff0000, v196
	v_lshlrev_b32_e32 v215, 16, v197
	v_and_b32_e32 v197, 0xffff0000, v197
	v_add_f32_e32 v170, v130, v170
	v_add_f32_e32 v194, v131, v194
	v_add_f32_e32 v171, v132, v171
	v_add_f32_e32 v195, v133, v195
	v_add_f32_e32 v214, v122, v214
	v_add_f32_e32 v196, v123, v196
	v_add_f32_e32 v215, v124, v215
	v_add_f32_e32 v197, v125, v197
	v_mul_f32_e32 v170, 0xbfb8aa3b, v170
	v_mul_f32_e32 v194, 0xbfb8aa3b, v194
	v_mul_f32_e32 v171, 0xbfb8aa3b, v171
	v_mul_f32_e32 v195, 0xbfb8aa3b, v195
	v_mul_f32_e32 v214, 0xbfb8aa3b, v214
	v_mul_f32_e32 v196, 0xbfb8aa3b, v196
	v_mul_f32_e32 v215, 0xbfb8aa3b, v215
	v_mul_f32_e32 v197, 0xbfb8aa3b, v197
	v_exp_f32_e32 v170, v170
	v_exp_f32_e32 v194, v194
	v_exp_f32_e32 v171, v171
	v_exp_f32_e32 v195, v195
	v_exp_f32_e32 v214, v214
	v_exp_f32_e32 v196, v196
	v_exp_f32_e32 v215, v215
	v_exp_f32_e32 v197, v197
	v_add_f32_e32 v170, 1.0, v170
	v_add_f32_e32 v194, 1.0, v194
	v_add_f32_e32 v171, 1.0, v171
	v_add_f32_e32 v195, 1.0, v195
	v_add_f32_e32 v214, 1.0, v214
	v_add_f32_e32 v196, 1.0, v196
	v_add_f32_e32 v215, 1.0, v215
	v_add_f32_e32 v197, 1.0, v197
	v_rcp_f32_e32 v170, v170
	v_rcp_f32_e32 v194, v194
	v_rcp_f32_e32 v171, v171
	v_rcp_f32_e32 v195, v195
	v_rcp_f32_e32 v214, v214
	v_rcp_f32_e32 v196, v196
	v_rcp_f32_e32 v215, v215
	v_rcp_f32_e32 v197, v197
	s_waitcnt vmcnt(7)
; __device__ __forceinline__ void unpack8(const v4u w, float (&o)[8]) { o[0] = bflo(w.x); o[1] = bfhi(w.x); o[2] = bflo(w.y); o[3] = bfhi(w.y); o[4] = bflo(w.z); o[5] = bfhi(w.z); o[6] = bflo(w.w); o[7] = bfhi(w.w); }
; __device__ __forceinline__ v4u pack8(const float (&o)[8]) { v4u w; w.x = pk2(o[0], o[1]); w.y = pk2(o[2], o[3]); w.z = pk2(o[4], o[5]); w.w = pk2(o[6], o[7]); return w; }
; __device__ __forceinline__ float sigmf(float x) { return __builtin_amdgcn_rcpf(1.f + __expf(-x)); }
;     __device__ __forceinline__ void operator()(const f32x4 (&acc)[2][2][4][2], const pg8::Unit& u, int wr, int wc, int fr, int fq_in) const {
;     ...
;                 for (int m = 0; m < 4; ++m) { const size_t row = (size_t)(row0 + ai * 128 + m * 16);
;                     gw_[m] = *(const v4u*)(Gt + row * (2 * D) + goff + col); pw_[m] = first ? (v4u){0u, 0u, 0u, 0u} : *(const v4u*)(O + row * D + col); }
;                 __builtin_amdgcn_sched_barrier(0);
; #pragma unroll
;                 for (int m = 0; m < 4; ++m) { const size_t row = (size_t)(row0 + ai * 128 + m * 16);
;                     float g0[8], p[8]; unpack8(gw_[m], g0); unpack8(pw_[m], p);
;                     float o[8];
; #pragma unroll
;                     for (int q = 0; q < 4; ++q) { o[q] = p[q] + sigmf(g0[q] + b0[q]) * acc[ai][bj][m][0][q]; o[4 + q] = p[4 + q] + sigmf(g0[4 + q] + b0[4 + q]) * acc[ai][bj][m][1][q]; }
;                     *(v4u*)(O + row * D + col) = pack8(o); }
	v_lshlrev_b32_e32 v221, 16, v240
	v_and_b32_e32 v240, 0xffff0000, v240
	v_lshlrev_b32_e32 v222, 16, v241
	v_and_b32_e32 v241, 0xffff0000, v241
	v_lshlrev_b32_e32 v223, 16, v242
	v_and_b32_e32 v242, 0xffff0000, v242
	v_lshlrev_b32_e32 v224, 16, v243
	v_and_b32_e32 v243, 0xffff0000, v243
	v_fma_f32 v38, v38, v170, v221
	v_fma_f32 v39, v39, v194, v240
	v_fma_f32 v40, v40, v171, v222
	v_fma_f32 v41, v41, v195, v241
	v_fma_f32 v34, v34, v214, v223
	v_fma_f32 v35, v35, v196, v242
	v_fma_f32 v36, v36, v215, v224
	v_fma_f32 v37, v37, v197, v243
	v_cvt_pk_bf16_f32 v38, v38, v39
	v_cvt_pk_bf16_f32 v39, v40, v41
	v_cvt_pk_bf16_f32 v40, v34, v35
	v_cvt_pk_bf16_f32 v41, v36, v37
	v_add_u32_e32 v253, 0xb0000, v226
	global_load_dwordx4 v[240:243], v253, s[4:5] offset:256 nt
	v_add_u32_e32 v225, 0x30000, v226
	global_store_dwordx4 v225, v[38:41], s[4:5] offset:256
	s_waitcnt vmcnt(29)
	v_lshlrev_b32_e32 v170, 16, v198
	v_and_b32_e32 v198, 0xffff0000, v198
	v_lshlrev_b32_e32 v171, 16, v199
	v_and_b32_e32 v199, 0xffff0000, v199
	v_lshlrev_b32_e32 v214, 16, v200
	v_and_b32_e32 v200, 0xffff0000, v200
	v_lshlrev_b32_e32 v215, 16, v201
	v_and_b32_e32 v201, 0xffff0000, v201
	v_add_f32_e32 v170, v130, v170
	v_add_f32_e32 v198, v131, v198
	v_add_f32_e32 v171, v132, v171
	v_add_f32_e32 v199, v133, v199
	v_add_f32_e32 v214, v122, v214
	v_add_f32_e32 v200, v123, v200
	v_add_f32_e32 v215, v124, v215
	v_add_f32_e32 v201, v125, v201
	v_mul_f32_e32 v170, 0xbfb8aa3b, v170
	v_mul_f32_e32 v198, 0xbfb8aa3b, v198
	v_mul_f32_e32 v171, 0xbfb8aa3b, v171
	v_mul_f32_e32 v199, 0xbfb8aa3b, v199
	v_mul_f32_e32 v214, 0xbfb8aa3b, v214
	v_mul_f32_e32 v200, 0xbfb8aa3b, v200
	v_mul_f32_e32 v215, 0xbfb8aa3b, v215
	v_mul_f32_e32 v201, 0xbfb8aa3b, v201
	v_exp_f32_e32 v170, v170
	v_exp_f32_e32 v198, v198
	v_exp_f32_e32 v171, v171
	v_exp_f32_e32 v199, v199
	v_exp_f32_e32 v214, v214
	v_exp_f32_e32 v200, v200
	v_exp_f32_e32 v215, v215
	v_exp_f32_e32 v201, v201
	v_add_f32_e32 v170, 1.0, v170
	v_add_f32_e32 v198, 1.0, v198
	v_add_f32_e32 v171, 1.0, v171
	v_add_f32_e32 v199, 1.0, v199
	v_add_f32_e32 v214, 1.0, v214
	v_add_f32_e32 v200, 1.0, v200
	v_add_f32_e32 v215, 1.0, v215
	v_add_f32_e32 v201, 1.0, v201
	v_rcp_f32_e32 v170, v170
	v_rcp_f32_e32 v198, v198
	v_rcp_f32_e32 v171, v171
	v_rcp_f32_e32 v199, v199
	v_rcp_f32_e32 v214, v214
	v_rcp_f32_e32 v200, v200
	v_rcp_f32_e32 v215, v215
	v_rcp_f32_e32 v201, v201
	s_waitcnt vmcnt(7)
	v_lshlrev_b32_e32 v221, 16, v228
	v_and_b32_e32 v228, 0xffff0000, v228
	v_lshlrev_b32_e32 v222, 16, v229
	v_and_b32_e32 v229, 0xffff0000, v229
	v_lshlrev_b32_e32 v223, 16, v230
	v_and_b32_e32 v230, 0xffff0000, v230
	v_lshlrev_b32_e32 v224, 16, v231
	v_and_b32_e32 v231, 0xffff0000, v231
	v_fma_f32 v30, v30, v170, v221
	v_fma_f32 v31, v31, v198, v228
	v_fma_f32 v32, v32, v171, v222
	v_fma_f32 v33, v33, v199, v229
	v_fma_f32 v26, v26, v214, v223
	v_fma_f32 v27, v27, v200, v230
	v_fma_f32 v28, v28, v215, v224
	v_fma_f32 v29, v29, v201, v231
	v_cvt_pk_bf16_f32 v30, v30, v31
	v_cvt_pk_bf16_f32 v31, v32, v33
	v_cvt_pk_bf16_f32 v32, v26, v27
	v_cvt_pk_bf16_f32 v33, v28, v29
	v_add_u32_e32 v225, 0x80000, v226
	global_store_dwordx4 v225, v[30:33], s[4:5] offset:256
	s_waitcnt vmcnt(29)
	v_lshlrev_b32_e32 v170, 16, v202
	v_and_b32_e32 v202, 0xffff0000, v202
	v_lshlrev_b32_e32 v171, 16, v203
	v_and_b32_e32 v203, 0xffff0000, v203
	v_lshlrev_b32_e32 v214, 16, v204
	v_and_b32_e32 v204, 0xffff0000, v204
	v_lshlrev_b32_e32 v215, 16, v205
	v_and_b32_e32 v205, 0xffff0000, v205
	v_add_f32_e32 v170, v130, v170
	v_add_f32_e32 v202, v131, v202
	v_add_f32_e32 v171, v132, v171
	v_add_f32_e32 v203, v133, v203
	v_add_f32_e32 v214, v122, v214
	v_add_f32_e32 v204, v123, v204
	v_add_f32_e32 v215, v124, v215
	v_add_f32_e32 v205, v125, v205
	v_mul_f32_e32 v170, 0xbfb8aa3b, v170
	v_mul_f32_e32 v202, 0xbfb8aa3b, v202
	v_mul_f32_e32 v171, 0xbfb8aa3b, v171
	v_mul_f32_e32 v203, 0xbfb8aa3b, v203
	v_mul_f32_e32 v214, 0xbfb8aa3b, v214
	v_mul_f32_e32 v204, 0xbfb8aa3b, v204
	v_mul_f32_e32 v215, 0xbfb8aa3b, v215
	v_mul_f32_e32 v205, 0xbfb8aa3b, v205
	v_exp_f32_e32 v170, v170
	v_exp_f32_e32 v202, v202
	v_exp_f32_e32 v171, v171
	v_exp_f32_e32 v203, v203
	v_exp_f32_e32 v214, v214
	v_exp_f32_e32 v204, v204
	v_exp_f32_e32 v215, v215
	v_exp_f32_e32 v205, v205
	v_add_f32_e32 v170, 1.0, v170
	v_add_f32_e32 v202, 1.0, v202
	v_add_f32_e32 v171, 1.0, v171
	v_add_f32_e32 v203, 1.0, v203
	v_add_f32_e32 v214, 1.0, v214
	v_add_f32_e32 v204, 1.0, v204
	v_add_f32_e32 v215, 1.0, v215
	v_add_f32_e32 v205, 1.0, v205
	v_rcp_f32_e32 v170, v170
	v_rcp_f32_e32 v202, v202
	v_rcp_f32_e32 v171, v171
	v_rcp_f32_e32 v203, v203
	v_rcp_f32_e32 v214, v214
	v_rcp_f32_e32 v204, v204
	v_rcp_f32_e32 v215, v215
	v_rcp_f32_e32 v205, v205
	s_waitcnt vmcnt(6)
; __device__ __forceinline__ void unpack8(const v4u w, float (&o)[8]) { o[0] = bflo(w.x); o[1] = bfhi(w.x); o[2] = bflo(w.y); o[3] = bfhi(w.y); o[4] = bflo(w.z); o[5] = bfhi(w.z); o[6] = bflo(w.w); o[7] = bfhi(w.w); }
; __device__ __forceinline__ v4u pack8(const float (&o)[8]) { v4u w; w.x = pk2(o[0], o[1]); w.y = pk2(o[2], o[3]); w.z = pk2(o[4], o[5]); w.w = pk2(o[6], o[7]); return w; }
; __device__ __forceinline__ float sigmf(float x) { return __builtin_amdgcn_rcpf(1.f + __expf(-x)); }
;     __device__ __forceinline__ void operator()(const f32x4 (&acc)[2][2][4][2], const pg8::Unit& u, int wr, int wc, int fr, int fq_in) const {
;     ...
;                 for (int m = 0; m < 4; ++m) { const size_t row = (size_t)(row0 + ai * 128 + m * 16);
;                     float g0[8], p[8]; unpack8(gw_[m], g0); unpack8(pw_[m], p);
;                     float o[8];
; #pragma unroll
;                     for (int q = 0; q < 4; ++q) { o[q] = p[q] + sigmf(g0[q] + b0[q]) * acc[ai][bj][m][0][q]; o[4 + q] = p[4 + q] + sigmf(g0[4 + q] + b0[4 + q]) * acc[ai][bj][m][1][q]; }
;                     *(v4u*)(O + row * D + col) = pack8(o); }
	v_lshlrev_b32_e32 v221, 16, v232
	v_and_b32_e32 v232, 0xffff0000, v232
	v_lshlrev_b32_e32 v222, 16, v233
	v_and_b32_e32 v233, 0xffff0000, v233
	v_lshlrev_b32_e32 v223, 16, v234
	v_and_b32_e32 v234, 0xffff0000, v234
	v_lshlrev_b32_e32 v224, 16, v235
	v_and_b32_e32 v235, 0xffff0000, v235
	v_fma_f32 v22, v22, v170, v221
	v_fma_f32 v23, v23, v202, v232
	v_fma_f32 v24, v24, v171, v222
	v_fma_f32 v25, v25, v203, v233
	v_fma_f32 v18, v18, v214, v223
	v_fma_f32 v19, v19, v204, v234
	v_fma_f32 v20, v20, v215, v224
	v_fma_f32 v21, v21, v205, v235
	v_cvt_pk_bf16_f32 v22, v22, v23
	v_cvt_pk_bf16_f32 v23, v24, v25
	v_cvt_pk_bf16_f32 v24, v18, v19
	v_cvt_pk_bf16_f32 v25, v20, v21
	v_add_u32_e32 v225, 0x90000, v226
	global_store_dwordx4 v225, v[22:25], s[4:5] offset:256
	s_waitcnt vmcnt(29)
	v_lshlrev_b32_e32 v170, 16, v206
	v_and_b32_e32 v206, 0xffff0000, v206
	v_lshlrev_b32_e32 v171, 16, v207
	v_and_b32_e32 v207, 0xffff0000, v207
	v_lshlrev_b32_e32 v214, 16, v208
	v_and_b32_e32 v208, 0xffff0000, v208
	v_lshlrev_b32_e32 v215, 16, v209
	v_and_b32_e32 v209, 0xffff0000, v209
	v_add_f32_e32 v170, v130, v170
	v_add_f32_e32 v206, v131, v206
	v_add_f32_e32 v171, v132, v171
	v_add_f32_e32 v207, v133, v207
	v_add_f32_e32 v214, v122, v214
	v_add_f32_e32 v208, v123, v208
	v_add_f32_e32 v215, v124, v215
	v_add_f32_e32 v209, v125, v209
	v_mul_f32_e32 v170, 0xbfb8aa3b, v170
	v_mul_f32_e32 v206, 0xbfb8aa3b, v206
	v_mul_f32_e32 v171, 0xbfb8aa3b, v171
	v_mul_f32_e32 v207, 0xbfb8aa3b, v207
	v_mul_f32_e32 v214, 0xbfb8aa3b, v214
	v_mul_f32_e32 v208, 0xbfb8aa3b, v208
	v_mul_f32_e32 v215, 0xbfb8aa3b, v215
	v_mul_f32_e32 v209, 0xbfb8aa3b, v209
	v_exp_f32_e32 v170, v170
	v_exp_f32_e32 v206, v206
	v_exp_f32_e32 v171, v171
	v_exp_f32_e32 v207, v207
	v_exp_f32_e32 v214, v214
	v_exp_f32_e32 v208, v208
	v_exp_f32_e32 v215, v215
	v_exp_f32_e32 v209, v209
	v_add_f32_e32 v170, 1.0, v170
	v_add_f32_e32 v206, 1.0, v206
	v_add_f32_e32 v171, 1.0, v171
	v_add_f32_e32 v207, 1.0, v207
	v_add_f32_e32 v214, 1.0, v214
	v_add_f32_e32 v208, 1.0, v208
	v_add_f32_e32 v215, 1.0, v215
	v_add_f32_e32 v209, 1.0, v209
	v_rcp_f32_e32 v170, v170
	v_rcp_f32_e32 v206, v206
	v_rcp_f32_e32 v171, v171
	v_rcp_f32_e32 v207, v207
	v_rcp_f32_e32 v214, v214
	v_rcp_f32_e32 v208, v208
	v_rcp_f32_e32 v215, v215
	v_rcp_f32_e32 v209, v209
	s_waitcnt vmcnt(5)
	v_lshlrev_b32_e32 v221, 16, v236
	v_and_b32_e32 v236, 0xffff0000, v236
	v_lshlrev_b32_e32 v222, 16, v237
	v_and_b32_e32 v237, 0xffff0000, v237
	v_lshlrev_b32_e32 v223, 16, v238
	v_and_b32_e32 v238, 0xffff0000, v238
	v_lshlrev_b32_e32 v224, 16, v239
	v_and_b32_e32 v239, 0xffff0000, v239
	v_fma_f32 v14, v14, v170, v221
	v_fma_f32 v15, v15, v206, v236
	v_fma_f32 v16, v16, v171, v222
	v_fma_f32 v17, v17, v207, v237
	v_fma_f32 v10, v10, v214, v223
	v_fma_f32 v11, v11, v208, v238
	v_fma_f32 v12, v12, v215, v224
	v_fma_f32 v13, v13, v209, v239
	v_cvt_pk_bf16_f32 v14, v14, v15
	v_cvt_pk_bf16_f32 v15, v16, v17
	v_cvt_pk_bf16_f32 v16, v10, v11
	v_cvt_pk_bf16_f32 v17, v12, v13
	v_add_u32_e32 v225, 0xa0000, v226
	global_store_dwordx4 v225, v[14:17], s[4:5] offset:256
	s_waitcnt vmcnt(29)
	v_lshlrev_b32_e32 v170, 16, v210
	v_and_b32_e32 v210, 0xffff0000, v210
	v_lshlrev_b32_e32 v171, 16, v211
	v_and_b32_e32 v211, 0xffff0000, v211
	v_lshlrev_b32_e32 v214, 16, v212
	v_and_b32_e32 v212, 0xffff0000, v212
	v_lshlrev_b32_e32 v215, 16, v213
	v_and_b32_e32 v213, 0xffff0000, v213
	v_add_f32_e32 v170, v130, v170
	v_add_f32_e32 v210, v131, v210
	v_add_f32_e32 v171, v132, v171
	v_add_f32_e32 v211, v133, v211
	v_add_f32_e32 v214, v122, v214
	v_add_f32_e32 v212, v123, v212
	v_add_f32_e32 v215, v124, v215
	v_add_f32_e32 v213, v125, v213
	v_mul_f32_e32 v170, 0xbfb8aa3b, v170
	v_mul_f32_e32 v210, 0xbfb8aa3b, v210
	v_mul_f32_e32 v171, 0xbfb8aa3b, v171
	v_mul_f32_e32 v211, 0xbfb8aa3b, v211
	v_mul_f32_e32 v214, 0xbfb8aa3b, v214
	v_mul_f32_e32 v212, 0xbfb8aa3b, v212
	v_mul_f32_e32 v215, 0xbfb8aa3b, v215
	v_mul_f32_e32 v213, 0xbfb8aa3b, v213
	v_exp_f32_e32 v170, v170
	v_exp_f32_e32 v210, v210
	v_exp_f32_e32 v171, v171
	v_exp_f32_e32 v211, v211
	v_exp_f32_e32 v214, v214
	v_exp_f32_e32 v212, v212
	v_exp_f32_e32 v215, v215
	v_exp_f32_e32 v213, v213
	v_add_f32_e32 v170, 1.0, v170
	v_add_f32_e32 v210, 1.0, v210
	v_add_f32_e32 v171, 1.0, v171
	v_add_f32_e32 v211, 1.0, v211
	v_add_f32_e32 v214, 1.0, v214
	v_add_f32_e32 v212, 1.0, v212
	v_add_f32_e32 v215, 1.0, v215
	v_add_f32_e32 v213, 1.0, v213
	v_rcp_f32_e32 v170, v170
	v_rcp_f32_e32 v210, v210
	v_rcp_f32_e32 v171, v171
	v_rcp_f32_e32 v211, v211
	v_rcp_f32_e32 v214, v214
	v_rcp_f32_e32 v212, v212
	v_rcp_f32_e32 v215, v215
	v_rcp_f32_e32 v213, v213
	s_waitcnt vmcnt(4)
	v_lshlrev_b32_e32 v221, 16, v240
	v_and_b32_e32 v240, 0xffff0000, v240
	v_lshlrev_b32_e32 v222, 16, v241
	v_and_b32_e32 v241, 0xffff0000, v241
	v_lshlrev_b32_e32 v223, 16, v242
	v_and_b32_e32 v242, 0xffff0000, v242
	v_lshlrev_b32_e32 v224, 16, v243
	v_and_b32_e32 v243, 0xffff0000, v243
	v_fma_f32 v6, v6, v170, v221
	v_fma_f32 v7, v7, v210, v240
	v_fma_f32 v8, v8, v171, v222
	v_fma_f32 v9, v9, v211, v241
	v_fma_f32 v2, v2, v214, v223
	v_fma_f32 v3, v3, v212, v242
	v_fma_f32 v4, v4, v215, v224
	v_fma_f32 v5, v5, v213, v243
	v_cvt_pk_bf16_f32 v6, v6, v7
	v_cvt_pk_bf16_f32 v7, v8, v9
	v_cvt_pk_bf16_f32 v8, v2, v3
	v_cvt_pk_bf16_f32 v9, v4, v5
	v_add_u32_e32 v225, 0xb0000, v226
	global_store_dwordx4 v225, v[6:9], s[4:5] offset:256
